# PROJ start staggered in 4 groups of CUs (bid>>3)&3 by 2 x s_sleep 110 per group step, to desynchronise epilogue store bursts
# speedup vs baseline: 1.0168x; 1.0117x over previous
.LBB0_269:
	s_cmp_lt_i32 s86, 4
	s_cselect_b64 s[20:21], -1, 0
	s_and_b64 s[0:1], s[20:21], s[0:1]
	s_andn2_b64 vcc, exec, s[0:1]
	v_writelane_b32 v255, s97, 8
	s_cbranch_vccnz .LBB0_801
	s_lshr_b32 s2, s94, 3
	s_and_b32 s2, s2, 3
	s_lshl_b32 s2, s2, 1
	s_cmp_eq_u32 s2, 0
	s_cbranch_scc1 .Lstg_done_proj
.Lstg_loop_proj:
	s_sleep 110
	s_sub_u32 s2, s2, 1
	s_cmp_lg_u32 s2, 0
	s_cbranch_scc1 .Lstg_loop_proj
